# same barrier; lane reads of the counter addresses reordered for a wider gap before the arrival atomic
# speedup vs baseline: 1.0013x; 1.0013x over previous
.LBB0_600:
	s_cmp_eq_u32 s2, 3
	s_cselect_b64 s[0:1], -1, 0
	v_writelane_b32 v253, s0, 63
	s_nop 1
	v_writelane_b32 v254, s1, 0
	s_and_b64 s[0:1], s[0:1], exec
	s_cselect_b32 s3, 0, s2
	s_lshl_b32 s0, s2, 3
	s_or_b32 s60, s0, 1
	v_writelane_b32 v254, s2, 1
	s_cmp_eq_u32 s3, 0
	v_writelane_b32 v254, s0, 2
	s_cselect_b64 s[0:1], -1, 0
	v_writelane_b32 v254, s0, 3
	s_cmp_lg_u32 s3, 0
	s_nop 0
	v_writelane_b32 v254, s1, 4
	v_writelane_b32 v254, s3, 5
	s_cbranch_scc1 .LBB0_1779
	v_readlane_b32 s6, v253, 3
	v_readlane_b32 s7, v253, 4
	s_cmp_lt_i32 s60, s6
	s_cselect_b64 s[0:1], -1, 0
	s_cmp_ge_i32 s60, s7
	s_cselect_b64 s[2:3], -1, 0
	s_or_b64 s[0:1], s[0:1], s[2:3]
	s_and_b64 vcc, exec, s[0:1]
	s_cbranch_vccnz .LBB0_968
	v_readlane_b32 s0, v254, 2
	s_cmp_lt_i32 s0, s6
	v_readlane_b32 s22, v254, 1
	s_cbranch_scc1 .LBB0_651
	s_waitcnt vmcnt(0)
	s_barrier
	s_mov_b64 s[0:1], exec
	v_readlane_b32 s2, v253, 1
	v_readlane_b32 s3, v253, 2
	s_and_b64 s[2:3], s[0:1], s[2:3]
	s_mov_b64 exec, s[2:3]
	s_cbranch_execz .LBB0_650
	v_readlane_b32 s8, v253, 7
	v_readlane_b32 s9, v253, 8
	v_readlane_b32 s4, v253, 36
	v_readlane_b32 s6, v253, 11
	v_readlane_b32 s7, v253, 12
	s_waitcnt vmcnt(0) lgkmcnt(0)
	v_mov_b32_e32 v1, s4
	ds_read2_b32 v[2:3], v1 offset1:1
	ds_read_b32 v7, v1 offset:8
	global_atomic_add v4, v87, v230, s[8:9] sc0
	s_waitcnt lgkmcnt(0)
	v_add_u32_e32 v7, 1, v7
	ds_write_b32 v1, v7 offset:8
	v_max_u32_e32 v2, 1, v2
	v_max_u32_e32 v3, 1, v3
	v_add_u32_e32 v6, 1, v7
	v_mul_lo_u32 v5, v6, v3
	v_mul_lo_u32 v6, v6, v2
	s_waitcnt vmcnt(0)
	v_add_u32_e32 v4, 1, v4
	v_cmp_ne_u32_e32 vcc, v4, v6
	s_cbranch_vccnz .Lxb_poll_0
	buffer_wbl2 sc1
	s_waitcnt vmcnt(0)
	global_atomic_add v87, v230, s[6:7]

.LBB0_968:
	v_readlane_b32 s0, v254, 2
	s_or_b32 s0, s0, 2
	s_cmp_lt_i32 s0, s6
	s_cselect_b64 s[2:3], -1, 0
	s_cmp_ge_i32 s0, s7
	s_cselect_b64 s[4:5], -1, 0
	s_or_b64 s[2:3], s[2:3], s[4:5]
	s_and_b64 vcc, exec, s[2:3]
	s_cbranch_vccnz .LBB0_1432
	s_cmp_le_i32 s0, s6
	s_cbranch_scc1 .LBB0_1008
	s_waitcnt vmcnt(0)
	s_waitcnt vmcnt(0) lgkmcnt(0)
	s_barrier
	s_mov_b64 s[0:1], exec
	v_readlane_b32 s2, v253, 1
	v_readlane_b32 s3, v253, 2
	s_and_b64 s[2:3], s[0:1], s[2:3]
	s_mov_b64 exec, s[2:3]
	s_cbranch_execz .LBB0_1007
	v_readlane_b32 s8, v253, 7
	v_readlane_b32 s9, v253, 8
	v_readlane_b32 s4, v253, 36
	v_readlane_b32 s6, v253, 11
	v_readlane_b32 s7, v253, 12
	s_waitcnt vmcnt(0) lgkmcnt(0)
	v_mov_b32_e32 v1, s4
	ds_read2_b32 v[2:3], v1 offset1:1
	ds_read_b32 v7, v1 offset:8
	global_atomic_add v4, v87, v230, s[8:9] sc0
	s_waitcnt lgkmcnt(0)
	v_add_u32_e32 v7, 1, v7
	ds_write_b32 v1, v7 offset:8
	v_max_u32_e32 v2, 1, v2
	v_max_u32_e32 v3, 1, v3
	v_add_u32_e32 v6, 1, v7
	v_mul_lo_u32 v5, v6, v3
	v_mul_lo_u32 v6, v6, v2
	s_waitcnt vmcnt(0)
	v_add_u32_e32 v4, 1, v4
	v_cmp_ne_u32_e32 vcc, v4, v6
	s_cbranch_vccnz .Lxb_poll_1
	buffer_wbl2 sc1
	s_waitcnt vmcnt(0)
	global_atomic_add v87, v230, s[6:7]

.LBB0_1432:
	v_readlane_b32 s0, v254, 2
	s_or_b32 s0, s0, 3
	s_cmp_lt_i32 s0, s6
	s_cselect_b64 s[2:3], -1, 0
	s_cmp_ge_i32 s0, s7
	s_cselect_b64 s[4:5], -1, 0
	s_or_b64 s[2:3], s[2:3], s[4:5]
	s_and_b64 vcc, exec, s[2:3]
	s_cbranch_vccnz .LBB0_1779
	v_readlane_b32 s2, v253, 3
	s_cmp_le_i32 s0, s2
	v_readlane_b32 s3, v253, 4
	s_cbranch_scc1 .LBB0_1472
	s_waitcnt vmcnt(0)
	s_waitcnt vmcnt(0) lgkmcnt(0)
	s_barrier
	s_mov_b64 s[0:1], exec
	v_readlane_b32 s2, v253, 1
	v_readlane_b32 s3, v253, 2
	s_and_b64 s[2:3], s[0:1], s[2:3]
	s_mov_b64 exec, s[2:3]
	s_cbranch_execz .LBB0_1471
	v_readlane_b32 s8, v253, 7
	v_readlane_b32 s9, v253, 8
	v_readlane_b32 s4, v253, 36
	v_readlane_b32 s6, v253, 11
	v_readlane_b32 s7, v253, 12
	s_waitcnt vmcnt(0) lgkmcnt(0)
	v_mov_b32_e32 v1, s4
	ds_read2_b32 v[2:3], v1 offset1:1
	ds_read_b32 v7, v1 offset:8
	global_atomic_add v4, v87, v230, s[8:9] sc0
	s_waitcnt lgkmcnt(0)
	v_add_u32_e32 v7, 1, v7
	ds_write_b32 v1, v7 offset:8
	v_max_u32_e32 v2, 1, v2
	v_max_u32_e32 v3, 1, v3
	v_add_u32_e32 v6, 1, v7
	v_mul_lo_u32 v5, v6, v3
	v_mul_lo_u32 v6, v6, v2
	s_waitcnt vmcnt(0)
	v_add_u32_e32 v4, 1, v4
	v_cmp_ne_u32_e32 vcc, v4, v6
	s_cbranch_vccnz .Lxb_poll_2
	buffer_wbl2 sc1
	s_waitcnt vmcnt(0)
	global_atomic_add v87, v230, s[6:7]

.LBB0_1779:
	v_readlane_b32 s0, v254, 5
	s_cmp_eq_u32 s0, 1
	s_cselect_b64 s[2:3], -1, 0
	v_writelane_b32 v254, s2, 6
	s_cmp_lg_u32 s0, 1
	s_nop 0
	v_writelane_b32 v254, s3, 7
	s_cbranch_scc1 .LBB0_2204
	v_readlane_b32 s4, v253, 3
	v_readlane_b32 s5, v253, 4
	s_cmp_lt_i32 s60, s4
	s_cselect_b64 s[0:1], -1, 0
	s_cmp_ge_i32 s60, s5
	s_cselect_b64 s[2:3], -1, 0
	s_or_b64 s[0:1], s[0:1], s[2:3]
	s_and_b64 vcc, exec, s[0:1]
	s_cbranch_vccnz .LBB0_1832
	v_readlane_b32 s0, v254, 2
	s_cmp_lt_i32 s0, s4
	s_cbranch_scc1 .LBB0_1820
	s_waitcnt vmcnt(0)
	s_waitcnt vmcnt(0) lgkmcnt(0)
	s_barrier
	s_mov_b64 s[0:1], exec
	v_readlane_b32 s2, v253, 1
	v_readlane_b32 s3, v253, 2
	v_readlane_b32 s18, v253, 61
	s_and_b64 s[2:3], s[0:1], s[2:3]
	v_readlane_b32 s19, v253, 62
	s_mov_b64 exec, s[2:3]
	s_cbranch_execz .LBB0_1819
	v_readlane_b32 s8, v253, 7
	v_readlane_b32 s9, v253, 8
	v_readlane_b32 s4, v253, 36
	v_readlane_b32 s6, v253, 11
	v_readlane_b32 s7, v253, 12
	s_waitcnt vmcnt(0) lgkmcnt(0)
	v_mov_b32_e32 v1, s4
	ds_read2_b32 v[2:3], v1 offset1:1
	ds_read_b32 v7, v1 offset:8
	global_atomic_add v4, v87, v230, s[8:9] sc0
	s_waitcnt lgkmcnt(0)
	v_add_u32_e32 v7, 1, v7
	ds_write_b32 v1, v7 offset:8
	v_max_u32_e32 v2, 1, v2
	v_max_u32_e32 v3, 1, v3
	v_add_u32_e32 v6, 1, v7
	v_mul_lo_u32 v5, v6, v3
	v_mul_lo_u32 v6, v6, v2
	s_waitcnt vmcnt(0)
	v_add_u32_e32 v4, 1, v4
	v_cmp_ne_u32_e32 vcc, v4, v6
	s_cbranch_vccnz .Lxb_poll_3
	buffer_wbl2 sc1
	s_waitcnt vmcnt(0)
	global_atomic_add v87, v230, s[6:7]

.LBB0_1832:
	v_readlane_b32 s0, v254, 2
	s_or_b32 s0, s0, 3
	s_cmp_lt_i32 s0, s4
	s_cselect_b64 s[2:3], -1, 0
	s_cmp_ge_i32 s0, s5
	s_cselect_b64 s[4:5], -1, 0
	s_or_b64 s[2:3], s[2:3], s[4:5]
	s_and_b64 vcc, exec, s[2:3]
	s_cbranch_vccnz .LBB0_2204
	v_readlane_b32 s2, v253, 3
	s_cmp_le_i32 s0, s2
	v_readlane_b32 s3, v253, 4
	s_cbranch_scc1 .LBB0_1872
	s_waitcnt vmcnt(0)
	s_waitcnt vmcnt(0) lgkmcnt(0)
	s_barrier
	s_mov_b64 s[0:1], exec
	v_readlane_b32 s2, v253, 1
	v_readlane_b32 s3, v253, 2
	v_readlane_b32 s18, v253, 61
	s_and_b64 s[2:3], s[0:1], s[2:3]
	v_readlane_b32 s19, v253, 62
	s_mov_b64 exec, s[2:3]
	s_cbranch_execz .LBB0_1871
	v_readlane_b32 s8, v253, 7
	v_readlane_b32 s9, v253, 8
	v_readlane_b32 s4, v253, 36
	v_readlane_b32 s6, v253, 11
	v_readlane_b32 s7, v253, 12
	s_waitcnt vmcnt(0) lgkmcnt(0)
	v_mov_b32_e32 v1, s4
	ds_read2_b32 v[2:3], v1 offset1:1
	ds_read_b32 v7, v1 offset:8
	global_atomic_add v4, v87, v230, s[8:9] sc0
	s_waitcnt lgkmcnt(0)
	v_add_u32_e32 v7, 1, v7
	ds_write_b32 v1, v7 offset:8
	v_max_u32_e32 v2, 1, v2
	v_max_u32_e32 v3, 1, v3
	v_add_u32_e32 v6, 1, v7
	v_mul_lo_u32 v5, v6, v3
	v_mul_lo_u32 v6, v6, v2
	s_waitcnt vmcnt(0)
	v_add_u32_e32 v4, 1, v4
	v_cmp_ne_u32_e32 vcc, v4, v6
	s_cbranch_vccnz .Lxb_poll_4
	buffer_wbl2 sc1
	s_waitcnt vmcnt(0)
	global_atomic_add v87, v230, s[6:7]

.LBB0_2204:
	v_readlane_b32 s0, v254, 5
	s_cmp_lg_u32 s0, 2
	s_cbranch_scc1 .LBB0_3126
	v_readlane_b32 s6, v253, 3
	v_readlane_b32 s7, v253, 4
	s_cmp_lt_i32 s60, s6
	s_cselect_b64 s[0:1], -1, 0
	s_cmp_ge_i32 s60, s7
	s_cselect_b64 s[2:3], -1, 0
	s_or_b64 s[0:1], s[0:1], s[2:3]
	s_and_b64 vcc, exec, s[0:1]
	s_cbranch_vccnz .LBB0_2673
	v_readlane_b32 s0, v254, 2
	v_readlane_b32 s18, v253, 61
	s_cmp_lt_i32 s0, s6
	v_readlane_b32 s19, v253, 62
	s_cbranch_scc1 .LBB0_2245
	s_waitcnt vmcnt(0)
	s_waitcnt vmcnt(0) lgkmcnt(0)
	s_barrier
	s_mov_b64 s[0:1], exec
	v_readlane_b32 s2, v253, 1
	v_readlane_b32 s3, v253, 2
	s_and_b64 s[2:3], s[0:1], s[2:3]
	s_mov_b64 exec, s[2:3]
	s_cbranch_execz .LBB0_2244
	v_readlane_b32 s8, v253, 7
	v_readlane_b32 s9, v253, 8
	v_readlane_b32 s4, v253, 36
	v_readlane_b32 s6, v253, 11
	v_readlane_b32 s7, v253, 12
	s_waitcnt vmcnt(0) lgkmcnt(0)
	v_mov_b32_e32 v1, s4
	ds_read2_b32 v[2:3], v1 offset1:1
	ds_read_b32 v7, v1 offset:8
	global_atomic_add v4, v87, v230, s[8:9] sc0
	s_waitcnt lgkmcnt(0)
	v_add_u32_e32 v7, 1, v7
	ds_write_b32 v1, v7 offset:8
	v_max_u32_e32 v2, 1, v2
	v_max_u32_e32 v3, 1, v3
	v_add_u32_e32 v6, 1, v7
	v_mul_lo_u32 v5, v6, v3
	v_mul_lo_u32 v6, v6, v2
	s_waitcnt vmcnt(0)
	v_add_u32_e32 v4, 1, v4
	v_cmp_ne_u32_e32 vcc, v4, v6
	s_cbranch_vccnz .Lxb_poll_5
	buffer_wbl2 sc1
	s_waitcnt vmcnt(0)
	global_atomic_add v87, v230, s[6:7]

.LBB0_2673:
	v_readlane_b32 s0, v254, 2
	s_or_b32 s0, s0, 2
	s_cmp_lt_i32 s0, s6
	s_cselect_b64 s[2:3], -1, 0
	s_cmp_ge_i32 s0, s7
	s_cselect_b64 s[4:5], -1, 0
	s_or_b64 s[2:3], s[2:3], s[4:5]
	s_and_b64 vcc, exec, s[2:3]
	s_cbranch_vccnz .LBB0_3029
	v_readlane_b32 s18, v253, 61
	s_cmp_le_i32 s0, s6
	v_readlane_b32 s19, v253, 62
	s_cbranch_scc1 .LBB0_2713
	s_waitcnt vmcnt(0)
	s_waitcnt vmcnt(0) lgkmcnt(0)
	s_barrier
	s_mov_b64 s[0:1], exec
	v_readlane_b32 s2, v253, 1
	v_readlane_b32 s3, v253, 2
	s_and_b64 s[2:3], s[0:1], s[2:3]
	s_mov_b64 exec, s[2:3]
	s_cbranch_execz .LBB0_2712
	v_readlane_b32 s8, v253, 7
	v_readlane_b32 s9, v253, 8
	v_readlane_b32 s4, v253, 36
	v_readlane_b32 s6, v253, 11
	v_readlane_b32 s7, v253, 12
	s_waitcnt vmcnt(0) lgkmcnt(0)
	v_mov_b32_e32 v1, s4
	ds_read2_b32 v[2:3], v1 offset1:1
	ds_read_b32 v7, v1 offset:8
	global_atomic_add v4, v87, v230, s[8:9] sc0
	s_waitcnt lgkmcnt(0)
	v_add_u32_e32 v7, 1, v7
	ds_write_b32 v1, v7 offset:8
	v_max_u32_e32 v2, 1, v2
	v_max_u32_e32 v3, 1, v3
	v_add_u32_e32 v6, 1, v7
	v_mul_lo_u32 v5, v6, v3
	v_mul_lo_u32 v6, v6, v2
	s_waitcnt vmcnt(0)
	v_add_u32_e32 v4, 1, v4
	v_cmp_ne_u32_e32 vcc, v4, v6
	s_cbranch_vccnz .Lxb_poll_6
	buffer_wbl2 sc1
	s_waitcnt vmcnt(0)
	global_atomic_add v87, v230, s[6:7]

.LBB0_3029:
	v_readlane_b32 s0, v254, 2
	s_or_b32 s0, s0, 3
	s_cmp_lt_i32 s0, s6
	s_cselect_b64 s[2:3], -1, 0
	s_cmp_ge_i32 s0, s7
	s_cselect_b64 s[4:5], -1, 0
	s_or_b64 s[2:3], s[2:3], s[4:5]
	s_and_b64 vcc, exec, s[2:3]
	s_cbranch_vccnz .LBB0_3126
	v_readlane_b32 s2, v253, 3
	v_readlane_b32 s18, v253, 61
	s_cmp_le_i32 s0, s2
	v_readlane_b32 s19, v253, 62
	v_readlane_b32 s3, v253, 4
	s_cbranch_scc1 .LBB0_3069
	s_waitcnt vmcnt(0)
	s_waitcnt vmcnt(0) lgkmcnt(0)
	s_barrier
	s_mov_b64 s[0:1], exec
	v_readlane_b32 s2, v253, 1
	v_readlane_b32 s3, v253, 2
	s_and_b64 s[2:3], s[0:1], s[2:3]
	s_mov_b64 exec, s[2:3]
	s_cbranch_execz .LBB0_3068
	v_readlane_b32 s8, v253, 7
	v_readlane_b32 s9, v253, 8
	v_readlane_b32 s4, v253, 36
	v_readlane_b32 s6, v253, 11
	v_readlane_b32 s7, v253, 12
	s_waitcnt vmcnt(0) lgkmcnt(0)
	v_mov_b32_e32 v1, s4
	ds_read2_b32 v[2:3], v1 offset1:1
	ds_read_b32 v7, v1 offset:8
	global_atomic_add v4, v87, v230, s[8:9] sc0
	s_waitcnt lgkmcnt(0)
	v_add_u32_e32 v7, 1, v7
	ds_write_b32 v1, v7 offset:8
	v_max_u32_e32 v2, 1, v2
	v_max_u32_e32 v3, 1, v3
	v_add_u32_e32 v6, 1, v7
	v_mul_lo_u32 v5, v6, v3
	v_mul_lo_u32 v6, v6, v2
	s_waitcnt vmcnt(0)
	v_add_u32_e32 v4, 1, v4
	v_cmp_ne_u32_e32 vcc, v4, v6
	s_cbranch_vccnz .Lxb_poll_7
	buffer_wbl2 sc1
	s_waitcnt vmcnt(0)
	global_atomic_add v87, v230, s[6:7]

.LBB0_3126:
	v_readlane_b32 s0, v254, 2
	s_or_b32 s0, s0, 4
	v_readlane_b32 s6, v253, 3
	v_readlane_b32 s7, v253, 4
	s_cmp_lt_i32 s0, s6
	s_cselect_b64 s[2:3], -1, 0
	s_cmp_ge_i32 s0, s7
	s_cselect_b64 s[4:5], -1, 0
	s_or_b64 s[2:3], s[2:3], s[4:5]
	v_readlane_b32 s58, v253, 61
	s_and_b64 vcc, exec, s[2:3]
	v_readlane_b32 s59, v253, 62
	s_cbranch_vccnz .LBB0_3186
	s_cmp_le_i32 s0, s6
	s_cbranch_scc1 .LBB0_3166
	s_waitcnt vmcnt(0)
	s_waitcnt vmcnt(0) lgkmcnt(0)
	s_barrier
	s_mov_b64 s[0:1], exec
	v_readlane_b32 s2, v253, 1
	v_readlane_b32 s3, v253, 2
	s_and_b64 s[2:3], s[0:1], s[2:3]
	s_mov_b64 exec, s[2:3]
	s_cbranch_execz .LBB0_3165
	v_readlane_b32 s8, v253, 7
	v_readlane_b32 s9, v253, 8
	v_readlane_b32 s4, v253, 36
	v_readlane_b32 s6, v253, 11
	v_readlane_b32 s7, v253, 12
	s_waitcnt vmcnt(0) lgkmcnt(0)
	v_mov_b32_e32 v1, s4
	ds_read2_b32 v[2:3], v1 offset1:1
	ds_read_b32 v7, v1 offset:8
	global_atomic_add v4, v87, v230, s[8:9] sc0
	s_waitcnt lgkmcnt(0)
	v_add_u32_e32 v7, 1, v7
	ds_write_b32 v1, v7 offset:8
	v_max_u32_e32 v2, 1, v2
	v_max_u32_e32 v3, 1, v3
	v_add_u32_e32 v6, 1, v7
	v_mul_lo_u32 v5, v6, v3
	v_mul_lo_u32 v6, v6, v2
	s_waitcnt vmcnt(0)
	v_add_u32_e32 v4, 1, v4
	v_cmp_ne_u32_e32 vcc, v4, v6
	s_cbranch_vccnz .Lxb_poll_8
	buffer_wbl2 sc1
	s_waitcnt vmcnt(0)
	global_atomic_add v87, v230, s[6:7]

.LBB0_3186:
	v_readlane_b32 s0, v254, 2
	s_or_b32 s0, s0, 5
	s_cmp_lt_i32 s0, s6
	s_cselect_b64 s[2:3], -1, 0
	s_cmp_ge_i32 s0, s7
	s_cselect_b64 s[4:5], -1, 0
	s_or_b64 s[2:3], s[2:3], s[4:5]
	v_readlane_b32 s76, v253, 59
	s_and_b64 vcc, exec, s[2:3]
	v_readlane_b32 s77, v253, 60
	s_cbranch_vccnz .LBB0_3269
	v_readlane_b32 s2, v253, 3
	s_cmp_le_i32 s0, s2
	v_readlane_b32 s3, v253, 4
	s_cbranch_scc1 .LBB0_3226
	s_waitcnt vmcnt(0)
	s_waitcnt vmcnt(0) lgkmcnt(0)
	s_barrier
	s_mov_b64 s[0:1], exec
	v_readlane_b32 s2, v253, 1
	v_readlane_b32 s3, v253, 2
	s_and_b64 s[2:3], s[0:1], s[2:3]
	s_mov_b64 exec, s[2:3]
	s_cbranch_execz .LBB0_3225
	v_readlane_b32 s8, v253, 7
	v_readlane_b32 s9, v253, 8
	v_readlane_b32 s4, v253, 36
	v_readlane_b32 s6, v253, 11
	v_readlane_b32 s7, v253, 12
	s_waitcnt vmcnt(0) lgkmcnt(0)
	v_mov_b32_e32 v1, s4
	ds_read2_b32 v[2:3], v1 offset1:1
	ds_read_b32 v7, v1 offset:8
	global_atomic_add v4, v87, v230, s[8:9] sc0
	s_waitcnt lgkmcnt(0)
	v_add_u32_e32 v7, 1, v7
	ds_write_b32 v1, v7 offset:8
	v_max_u32_e32 v2, 1, v2
	v_max_u32_e32 v3, 1, v3
	v_add_u32_e32 v6, 1, v7
	v_mul_lo_u32 v5, v6, v3
	v_mul_lo_u32 v6, v6, v2
	s_waitcnt vmcnt(0)
	v_add_u32_e32 v4, 1, v4
	v_cmp_ne_u32_e32 vcc, v4, v6
	s_cbranch_vccnz .Lxb_poll_9
	buffer_wbl2 sc1
	s_waitcnt vmcnt(0)
	global_atomic_add v87, v230, s[6:7]

.LBB0_3269:
	v_readlane_b32 s0, v254, 2
	s_or_b32 s0, s0, 6
	v_readlane_b32 s12, v253, 3
	v_readlane_b32 s13, v253, 4
	s_cmp_lt_i32 s0, s12
	s_cselect_b64 s[2:3], -1, 0
	s_cmp_ge_i32 s0, s13
	s_cselect_b64 s[4:5], -1, 0
	s_or_b64 s[2:3], s[2:3], s[4:5]
	s_and_b64 vcc, exec, s[2:3]
	s_cbranch_vccnz .LBB0_3391
	s_cmp_le_i32 s0, s12
	s_cbranch_scc1 .LBB0_3309
	s_waitcnt vmcnt(0)
	s_waitcnt vmcnt(0) lgkmcnt(0)
	s_barrier
	s_mov_b64 s[0:1], exec
	v_readlane_b32 s2, v253, 1
	v_readlane_b32 s3, v253, 2
	s_and_b64 s[2:3], s[0:1], s[2:3]
	s_mov_b64 exec, s[2:3]
	s_cbranch_execz .LBB0_3308
	v_readlane_b32 s8, v253, 7
	v_readlane_b32 s9, v253, 8
	v_readlane_b32 s4, v253, 36
	v_readlane_b32 s6, v253, 11
	v_readlane_b32 s7, v253, 12
	s_waitcnt vmcnt(0) lgkmcnt(0)
	v_mov_b32_e32 v1, s4
	ds_read2_b32 v[2:3], v1 offset1:1
	ds_read_b32 v7, v1 offset:8
	global_atomic_add v4, v87, v230, s[8:9] sc0
	s_waitcnt lgkmcnt(0)
	v_add_u32_e32 v7, 1, v7
	ds_write_b32 v1, v7 offset:8
	v_max_u32_e32 v2, 1, v2
	v_max_u32_e32 v3, 1, v3
	v_add_u32_e32 v6, 1, v7
	v_mul_lo_u32 v5, v6, v3
	v_mul_lo_u32 v6, v6, v2
	s_waitcnt vmcnt(0)
	v_add_u32_e32 v4, 1, v4
	v_cmp_ne_u32_e32 vcc, v4, v6
	s_cbranch_vccnz .Lxb_poll_10
	buffer_wbl2 sc1
	s_waitcnt vmcnt(0)
	global_atomic_add v87, v230, s[6:7]

.LBB0_3391:
	v_readlane_b32 s0, v254, 2
	s_or_b32 s0, s0, 7
	s_cmp_lt_i32 s0, s12
	s_cselect_b64 s[2:3], -1, 0
	s_cmp_ge_i32 s0, s13
	s_cselect_b64 s[4:5], -1, 0
	s_or_b64 s[2:3], s[2:3], s[4:5]
	s_and_b64 vcc, exec, s[2:3]
	s_cbranch_vccnz .LBB0_3493
	s_cmp_le_i32 s0, s12
	s_cbranch_scc1 .LBB0_3431
	s_waitcnt vmcnt(0)
	s_waitcnt vmcnt(0) lgkmcnt(0)
	s_barrier
	s_mov_b64 s[0:1], exec
	v_readlane_b32 s2, v253, 1
	v_readlane_b32 s3, v253, 2
	s_and_b64 s[2:3], s[0:1], s[2:3]
	s_mov_b64 exec, s[2:3]
	s_cbranch_execz .LBB0_3430
	v_readlane_b32 s8, v253, 7
	v_readlane_b32 s9, v253, 8
	v_readlane_b32 s4, v253, 36
	v_readlane_b32 s6, v253, 11
	v_readlane_b32 s7, v253, 12
	s_waitcnt vmcnt(0) lgkmcnt(0)
	v_mov_b32_e32 v1, s4
	ds_read2_b32 v[2:3], v1 offset1:1
	ds_read_b32 v7, v1 offset:8
	global_atomic_add v4, v87, v230, s[8:9] sc0
	s_waitcnt lgkmcnt(0)
	v_add_u32_e32 v7, 1, v7
	ds_write_b32 v1, v7 offset:8
	v_max_u32_e32 v2, 1, v2
	v_max_u32_e32 v3, 1, v3
	v_add_u32_e32 v6, 1, v7
	v_mul_lo_u32 v5, v6, v3
	v_mul_lo_u32 v6, v6, v2
	s_waitcnt vmcnt(0)
	v_add_u32_e32 v4, 1, v4
	v_cmp_ne_u32_e32 vcc, v4, v6
	s_cbranch_vccnz .Lxb_poll_11
	buffer_wbl2 sc1
	s_waitcnt vmcnt(0)
	global_atomic_add v87, v230, s[6:7]

.LBB0_3494:
	v_readlane_b32 s2, v253, 3
	s_cmp_le_i32 s0, s2
	v_readlane_b32 s3, v253, 4
	s_cbranch_scc1 .LBB0_3533
	s_waitcnt vmcnt(0)
	s_waitcnt vmcnt(0) lgkmcnt(0)
	s_barrier
	s_mov_b64 s[0:1], exec
	v_readlane_b32 s2, v253, 1
	v_readlane_b32 s3, v253, 2
	s_and_b64 s[2:3], s[0:1], s[2:3]
	s_mov_b64 exec, s[2:3]
	s_cbranch_execz .LBB0_3532
	v_readlane_b32 s8, v253, 7
	v_readlane_b32 s9, v253, 8
	v_readlane_b32 s4, v253, 36
	v_readlane_b32 s6, v253, 11
	v_readlane_b32 s7, v253, 12
	s_waitcnt vmcnt(0) lgkmcnt(0)
	v_mov_b32_e32 v1, s4
	ds_read2_b32 v[2:3], v1 offset1:1
	ds_read_b32 v7, v1 offset:8
	global_atomic_add v4, v87, v230, s[8:9] sc0
	s_waitcnt lgkmcnt(0)
	v_add_u32_e32 v7, 1, v7
	ds_write_b32 v1, v7 offset:8
	v_max_u32_e32 v2, 1, v2
	v_max_u32_e32 v3, 1, v3
	v_add_u32_e32 v6, 1, v7
	v_mul_lo_u32 v5, v6, v3
	v_mul_lo_u32 v6, v6, v2
	s_waitcnt vmcnt(0)
	v_add_u32_e32 v4, 1, v4
	v_cmp_ne_u32_e32 vcc, v4, v6
	s_cbranch_vccnz .Lxb_poll_12
	buffer_wbl2 sc1
	s_waitcnt vmcnt(0)
	global_atomic_add v87, v230, s[6:7]
